# code placement: one 4-byte pad at the outproj phase entry so the outproj and MoE K-loops start 8-byte aligned
# baseline (speedup 1.0000x reference)
.LBB0_1301:
	s_nop 0
	v_readlane_b32 s0, v251, 3
	v_readlane_b32 s2, v251, 5
	v_readlane_b32 s1, v251, 4
	v_readlane_b32 s3, v251, 6
	s_cmp_ge_i32 s16, s2
	s_cselect_b64 s[0:1], -1, 0
	s_cmp_lt_i32 s16, s3
	s_cselect_b64 s[2:3], -1, 0
	s_and_b64 s[2:3], s[0:1], s[2:3]
	s_mov_b64 s[0:1], -1
	s_and_b64 vcc, exec, s[2:3]
	s_cbranch_vccnz .LBB0_1303
	s_add_i32 s16, s97, 7
	s_mov_b64 s[0:1], 0
